# prologue de-serialisation (PEER/LN vector caches, rope copy) with the PEER loop kept at its original 8-byte instruction phase
# baseline (speedup 1.0000x reference)
.LBB0_708:
	s_or_b64 exec, exec, s[4:5]
	s_load_dwordx2 s[50:51], s[0:1], 0xa8
	s_waitcnt vmcnt(0)
	v_lshlrev_b32_e32 v5, 6, v2
	v_lshrrev_b32_e32 v4, 3, v2
	v_and_b32_e32 v5, 0x1c0, v5
	s_cmp_lg_u32 s36, 3
	v_add_lshl_u32 v6, v5, v4, 4
	s_cselect_b64 s[96:97], -1, 0
	v_lshlrev_b32_e32 v4, 2, v2
	s_waitcnt lgkmcnt(0)
	s_add_u32 s4, s50, 0x100000
	v_readlane_b32 s6, v253, 15
	v_ashrrev_i32_e32 v5, 31, v4
	s_addc_u32 s5, s51, 0
	v_add_u32_e32 v7, s6, v6
	s_load_dwordx4 s[40:43], s[0:1], 0x90
	v_lshlrev_b32_e32 v8, 4, v2
	s_cmp_lg_u32 s36, 3
	s_cselect_b32 s9, 1, 0
	s_add_i32 s9, s36, s9
	s_mul_i32 s8, s36, 3
	s_mul_i32 s9, s9, 3
	s_add_i32 s37, s8, 0
	s_mul_i32 s37, s37, 0xc000
	s_add_i32 s37, s37, 0xa000
	s_add_u32 s52, s4, s37
	s_addc_u32 s53, s5, 0
	global_load_dwordx4 v[24:27], v8, s[52:53]
	s_add_i32 s37, s8, 1
	s_mul_i32 s37, s37, 0xc000
	s_add_i32 s37, s37, 0xa000
	s_add_u32 s52, s4, s37
	s_addc_u32 s53, s5, 0
	global_load_dwordx4 v[28:31], v8, s[52:53]
	s_add_i32 s37, s8, 2
	s_mul_i32 s37, s37, 0xc000
	s_add_i32 s37, s37, 0xa000
	s_add_u32 s52, s4, s37
	s_addc_u32 s53, s5, 0
	global_load_dwordx4 v[32:35], v8, s[52:53]
	s_add_i32 s37, s9, 0
	s_mul_i32 s37, s37, 0xc000
	s_add_u32 s52, s4, s37
	s_addc_u32 s53, s5, 0
	global_load_dwordx4 v[36:39], v8, s[52:53]
	s_add_i32 s37, s9, 1
	s_mul_i32 s37, s37, 0xc000
	s_add_u32 s52, s4, s37
	s_addc_u32 s53, s5, 0
	global_load_dwordx4 v[40:43], v8, s[52:53]
	s_add_i32 s37, s9, 2
	s_mul_i32 s37, s37, 0xc000
	s_add_u32 s52, s4, s37
	s_addc_u32 s53, s5, 0
	global_load_dwordx4 v[44:47], v8, s[52:53]
	s_add_i32 s37, s9, 0
	s_mul_i32 s37, s37, 0xc000
	s_add_i32 s37, s37, 0x2000
	s_add_u32 s52, s4, s37
	s_addc_u32 s53, s5, 0
	global_load_dwordx4 v[48:51], v8, s[52:53]
	s_add_i32 s37, s9, 1
	s_mul_i32 s37, s37, 0xc000
	s_add_i32 s37, s37, 0x2000
	s_add_u32 s52, s4, s37
	s_addc_u32 s53, s5, 0
	global_load_dwordx4 v[52:55], v8, s[52:53]
	s_add_i32 s37, s9, 2
	s_mul_i32 s37, s37, 0xc000
	s_add_i32 s37, s37, 0x2000
	s_add_u32 s52, s4, s37
	s_addc_u32 s53, s5, 0
	global_load_dwordx4 v[56:59], v8, s[52:53]
	s_waitcnt lgkmcnt(0)
	s_lshl_b32 s6, s36, 11
	s_lshl_b64 s[4:5], s[6:7], 2
	s_add_u32 s8, s40, s4
	s_addc_u32 s9, s41, s5
	global_load_dwordx4 v[60:63], v8, s[8:9]
	s_add_u32 s4, s42, s4
	s_addc_u32 s5, s43, s5
	global_load_dwordx4 v[64:67], v8, s[4:5]
	s_lshl_b32 s6, s36, 6
	v_and_b32_e32 v21, 63, v2
	v_cmp_eq_u32_e64 s[40:41], 0, v21
	s_lshl_b64 s[4:5], s[6:7], 2
	v_readlane_b32 s6, v254, 50
	s_add_u32 s66, s6, s4
	v_readlane_b32 s4, v254, 51
	s_addc_u32 s67, s4, s5
	v_add_u32_e32 v9, 0x8000, v7
	v_add_u32_e32 v11, 0x1c200, v6
	v_add_u32_e32 v12, 0x1e200, v6
	s_waitcnt vmcnt(10)
	ds_write_b128 v7, v[24:27]
	s_waitcnt vmcnt(9)
	ds_write_b128 v7, v[28:31] offset:8192
	s_waitcnt vmcnt(8)
	ds_write_b128 v7, v[32:35] offset:16384
	s_waitcnt vmcnt(7)
	ds_write_b128 v7, v[36:39] offset:24576
	s_waitcnt vmcnt(6)
	ds_write_b128 v9, v[40:43]
	s_waitcnt vmcnt(5)
	ds_write_b128 v9, v[44:47] offset:8192
	s_waitcnt vmcnt(4)
	ds_write_b128 v9, v[48:51] offset:16384
	s_waitcnt vmcnt(3)
	ds_write_b128 v9, v[52:55] offset:24576
	s_waitcnt vmcnt(2)
	ds_write_b128 v9, v[56:59] offset:32768
	s_waitcnt vmcnt(1)
	ds_write_b128 v11, v[60:63]
	s_waitcnt vmcnt(0)
	ds_write_b128 v12, v[64:67]
	v_mov_b32_e32 v4, 0
	s_waitcnt lgkmcnt(0)
	s_barrier
	v_readlane_b32 s6, v254, 3
	s_lshr_b32 s4, s27, 6
	s_add_i32 s6, s6, s4
	v_readlane_b32 s44, v253, 31
	v_readlane_b32 s45, v253, 32
	s_mov_b32 s88, s6
	s_cmp_lt_i32 s88, s26
	v_lshlrev_b32_e32 v20, 6, v21
	s_cselect_b64 s[4:5], -1, 0
	s_cmp_ge_i32 s88, s26
	v_and_b32_e32 v24, 0xf00, v20
	v_and_b32_e32 v22, 0xc0, v20
	s_cbranch_scc1 .LBB0_716
	s_ashr_i32 s89, s88, 31
	s_lshl_b64 s[8:9], s[88:89], 12
	s_add_u32 s8, s50, s8
	s_addc_u32 s9, s51, s9
	v_mov_b32_e32 v25, v3
	v_lshl_add_u64 v[4:5], s[8:9], 0, v[24:25]
	v_mov_b32_e32 v23, v3
	v_lshl_add_u64 v[4:5], v[4:5], 0, v[22:23]
	s_mov_b64 s[8:9], 0x24d00000
	s_mov_b32 s6, 0x24d00000
	v_lshl_add_u64 v[16:17], v[4:5], 0, s[8:9]
	v_add_co_u32_e32 v4, vcc, s6, v4
	s_nop 1
	v_addc_co_u32_e32 v5, vcc, 0, v5, vcc
	global_load_dwordx4 v[4:7], v[4:5], off
	s_nop 0
	global_load_dwordx4 v[8:11], v[16:17], off offset:48
	global_load_dwordx4 v[12:15], v[16:17], off offset:32
	s_nop 0
	global_load_dwordx4 v[16:19], v[16:17], off offset:16
	s_nop 0
